# router-phase pool: router workgroups join the conversion pool after their unit (same fall-through as the w_in phase), with the 80/20 split
# baseline (speedup 1.0000x reference)
; #define LAS __attribute__((address_space(3)))
; DI int lane_id() { int l; asm volatile("v_mbcnt_lo_u32_b32 %0, -1, 0\n\tv_mbcnt_hi_u32_b32 %0, -1, %0" : "=v"(l)); return l; }
; DI int wave_in_wg() { return __builtin_amdgcn_readfirstlane(((const LAS int*)((LAS unsigned char*)lds_raw + LDS_CTL_OFF + 1024))[hw_wave_slot()]); }
; #define PHASE(k, ...) do { if (IN(k)) { __VA_ARGS__ if ((REP_MASK >> (k)) & 1) { GRID_BAR(); __VA_ARGS__ } } SEAM(k); } while (0)
; DI void conv_pool(const Params& P, LAS unsigned char* lds, int pool, int blk_lo, int blk_hi) {
;     const int wid = wave_in_wg(), lane = lane_id();
;     LAS float* scr = (LAS float*)(lds + wid * 16896);
;     unsigned* ctr = (unsigned*)(P.ws + WS_CTL) + CW_POOL + pool * 64;
;     const int CV_NBLK = blk_hi;
;     auto claim = [&]() -> int { unsigned v_ = 0u; if (lane == 0) v_ = __hip_atomic_fetch_add(ctr, 1u, __ATOMIC_RELAXED, __HIP_MEMORY_SCOPE_AGENT); return blk_lo + (int)__builtin_amdgcn_readfirstlane(v_); };
;     const int blk = claim(); if (blk >= CV_NBLK) return;
; __global__ void __launch_bounds__(512, 2) hymba_fwd(Params P) {
;     ...
;     PHASE(9, { SchedRouter S{P.ws, G, bid}; pg8::EpiLogits E{P.in[I_BR], (const float*)(P.ws + WS_RSTD), (const float*)(P.ws + WS_CBR)}; pg8::gemm_phase<pg8::EpiLogits, SchedRouter, true, true>(lds, P.ws, 2 * D, S, E);
;                if (slots && bid >= 128) conv_pool(P, lds, 1, CV_NBLK_A, CV_NBLK_ALL);
.LBB0_1111:
	s_mov_b32 s0, s60
	v_writelane_b32 v254, s0, 0
	s_cmpk_lt_i32 s60, 0x80
	s_nop 0
	v_writelane_b32 v254, s1, 1
	s_mov_b64 s[0:1], 0
	s_xor_b64 s[2:3], s[88:89], -1
	s_or_b64 s[0:1], s[0:1], s[2:3]
	s_and_b64 vcc, exec, s[0:1]
	s_cbranch_vccnz .LBB0_1136
	s_getreg_b32 s0, hwreg(HW_REG_HW_ID, 0, 6)
	s_and_b32 s0, s0, 63
	s_lshl_b32 s0, s0, 2
	s_add_i32 s0, s0, 0
	s_add_i32 s0, s0, 0x24400
	v_mov_b32_e32 v0, s0
	ds_read_b32 v1, v0
	v_readlane_b32 s0, v254, 2
	v_readlane_b32 s2, v254, 4
	v_readlane_b32 s1, v254, 3
	v_readlane_b32 s3, v254, 5
	s_add_u32 s4, s2, 0x14100
	v_mov_b32_e32 v0, 0
	v_mbcnt_lo_u32_b32 v56, -1, 0
	v_mbcnt_hi_u32_b32 v56, -1, v56
	s_addc_u32 s5, s3, 0
	s_waitcnt lgkmcnt(0)
	v_readfirstlane_b32 s12, v1
	v_cmp_eq_u32_e64 s[0:1], 0, v56
	s_and_saveexec_b64 s[2:3], s[0:1]
	s_cbranch_execz .LBB0_1116
	s_mov_b64 s[10:11], exec
	v_mbcnt_lo_u32_b32 v0, s10, 0
	v_mbcnt_hi_u32_b32 v0, s11, v0
	v_cmp_eq_u32_e32 vcc, 0, v0
	s_and_saveexec_b64 s[6:7], vcc
	s_cbranch_execz .LBB0_1115
	s_bcnt1_i32_b64 s10, s[10:11]
	v_mov_b32_e32 v1, 0
	v_mov_b32_e32 v2, s10
	global_atomic_add v1, v1, v2, s[4:5] sc0
